# v4 + static s_setprio 1 for waves 4-7 during latency-bound phases P3, P4, P12
# speedup vs baseline: 1.0952x; 1.0061x over previous
.LBB0_335:
	v_readfirstlane_b32 s99, v0
	s_lshr_b32 s99, s99, 6
	s_cmp_lt_u32 s99, 4
	s_cbranch_scc1 .Lprio_skip9401
	s_setprio 1

.LBB0_610:
	s_setprio 0
	v_readlane_b32 s2, v250, 40
	v_readlane_b32 s3, v250, 41
	s_cmp_lt_i32 s2, 6
	s_cselect_b64 s[2:3], -1, 0
	s_and_b64 s[0:1], s[2:3], s[0:1]
	s_andn2_b64 vcc, exec, s[0:1]
	s_cbranch_vccnz .LBB0_631
	s_cmpk_gt_i32 s74, 0xff
	v_readfirstlane_b32 s26, v0
	s_cbranch_scc1 .LBB0_631
	s_ashr_i32 s27, s74, 31
	s_lshr_b32 s0, s27, 29
	s_add_i32 s5, s74, s0
	s_and_b32 s0, s5, -8
	s_sub_i32 s4, s74, s0
	s_cmp_gt_i32 s4, -1
	s_cbranch_scc0 .LBB0_614
	s_lshl_b32 s6, s4, 5
	s_cbranch_execz .LBB0_615
	s_branch .LBB0_616

.LBB0_1463:
	s_setprio 0
	v_readlane_b32 s4, v250, 40
	v_readlane_b32 s5, v250, 41
	s_cmp_lt_i32 s4, 14
	s_cselect_b64 s[4:5], -1, 0
	s_and_b64 s[2:3], s[4:5], s[2:3]
	s_andn2_b64 vcc, exec, s[2:3]
	s_cbranch_vccnz .LBB0_1468
	v_lshl_or_b32 v1, s74, 9, v0
	s_mov_b32 s2, 0x100000
	v_cmp_gt_i32_e32 vcc, s2, v1
	s_and_saveexec_b64 s[6:7], vcc
	s_cbranch_execz .LBB0_1467
	s_waitcnt vmcnt(0)
	v_and_b32_e32 v2, 0x7f, v0
	v_lshlrev_b32_e32 v2, 3, v2
	v_mov_b32_e32 v3, 0
	v_lshrrev_b32_e32 v6, 1, v0
	s_add_u32 s2, s78, 0x48500000
	v_lshl_add_u64 v[4:5], s[78:79], 0, v[2:3]
	s_mov_b64 s[8:9], 0x4b700000
	v_and_b32_e32 v6, 60, v6
	v_mov_b32_e32 v7, v3
	s_addc_u32 s3, s79, 0
	v_lshl_add_u64 v[4:5], v[4:5], 0, s[8:9]
	v_lshl_add_u64 v[6:7], s[78:79], 0, v[6:7]
	s_mov_b64 s[8:9], 0x4b500000
	s_lshl_b32 s11, s97, 9
	v_lshl_add_u64 v[6:7], v[6:7], 0, s[8:9]
	s_mov_b64 s[8:9], 0
	s_movk_i32 s12, 0xc0
	s_movk_i32 s13, 0x1800
	v_mov_b64_e32 v[8:9], s[2:3]
	v_lshlrev_b32_e32 v2, 1, v2
	s_movk_i32 s14, 0x1000
	s_mov_b32 s10, 0x41800000
	s_mov_b32 s15, 0xfffff

	.amdhsa_kernel _Z8yoco_fwd4Args
		.amdhsa_group_segment_fixed_size 0
		.amdhsa_private_segment_fixed_size 0
		.amdhsa_kernarg_size 504
		.amdhsa_user_sgpr_count 2
		.amdhsa_user_sgpr_dispatch_ptr 0
		.amdhsa_user_sgpr_queue_ptr 0
		.amdhsa_user_sgpr_kernarg_segment_ptr 1
		.amdhsa_user_sgpr_dispatch_id 0
		.amdhsa_user_sgpr_kernarg_preload_length 0
		.amdhsa_user_sgpr_kernarg_preload_offset 0
		.amdhsa_user_sgpr_private_segment_size 0
		.amdhsa_uses_dynamic_stack 0
		.amdhsa_enable_private_segment 0
		.amdhsa_system_sgpr_workgroup_id_x 1
		.amdhsa_system_sgpr_workgroup_id_y 0
		.amdhsa_system_sgpr_workgroup_id_z 0
		.amdhsa_system_sgpr_workgroup_info 0
		.amdhsa_system_vgpr_workitem_id 0
		.amdhsa_next_free_vgpr 256
		.amdhsa_next_free_sgpr 100
		.amdhsa_accum_offset 256
		.amdhsa_reserve_vcc 1
		.amdhsa_float_round_mode_32 0
		.amdhsa_float_round_mode_16_64 0
		.amdhsa_float_denorm_mode_32 3
		.amdhsa_float_denorm_mode_16_64 3
		.amdhsa_dx10_clamp 1
		.amdhsa_ieee_mode 1
		.amdhsa_fp16_overflow 0
		.amdhsa_tg_split 0
		.amdhsa_exception_fp_ieee_invalid_op 0
		.amdhsa_exception_fp_denorm_src 0
		.amdhsa_exception_fp_ieee_div_zero 0
		.amdhsa_exception_fp_ieee_overflow 0
		.amdhsa_exception_fp_ieee_underflow 0
		.amdhsa_exception_fp_ieee_inexact 0
		.amdhsa_exception_int_div_zero 0
	.end_amdhsa_kernel

amdhsa.kernels:
  - .agpr_count:     0
    .args:
      - .offset:         0
        .size:           248
        .value_kind:     by_value
      - .offset:         248
        .size:           4
        .value_kind:     hidden_block_count_x
      - .offset:         252
        .size:           4
        .value_kind:     hidden_block_count_y
      - .offset:         256
        .size:           4
        .value_kind:     hidden_block_count_z
      - .offset:         260
        .size:           2
        .value_kind:     hidden_group_size_x
      - .offset:         262
        .size:           2
        .value_kind:     hidden_group_size_y
      - .offset:         264
        .size:           2
        .value_kind:     hidden_group_size_z
      - .offset:         266
        .size:           2
        .value_kind:     hidden_remainder_x
      - .offset:         268
        .size:           2
        .value_kind:     hidden_remainder_y
      - .offset:         270
        .size:           2
        .value_kind:     hidden_remainder_z
      - .offset:         288
        .size:           8
        .value_kind:     hidden_global_offset_x
      - .offset:         296
        .size:           8
        .value_kind:     hidden_global_offset_y
      - .offset:         304
        .size:           8
        .value_kind:     hidden_global_offset_z
      - .offset:         312
        .size:           2
        .value_kind:     hidden_grid_dims
      - .offset:         368
        .size:           4
        .value_kind:     hidden_dynamic_lds_size
    .group_segment_fixed_size: 0
    .kernarg_segment_align: 8
    .kernarg_segment_size: 504
    .language:       OpenCL C
    .language_version:
      - 2
      - 0
    .max_flat_workgroup_size: 512
    .name:           _Z8yoco_fwd4Args
    .private_segment_fixed_size: 0
    .sgpr_count:     106
    .sgpr_spill_count: 440
    .symbol:         _Z8yoco_fwd4Args.kd
    .uniform_work_group_size: 1
    .uses_dynamic_stack: false
    .vgpr_count:     256
    .vgpr_spill_count: 0
    .wavefront_size: 64
